# grid barrier: non-leader L1 invalidate issued before the release poll; on top of stage 1b rewrite
# speedup vs baseline: 1.0026x; 1.0024x over previous
.LBB0_120:
	s_lshl_b32 s7, s6, 2
	s_add_u32 s8, s4, s7
	s_addc_u32 s9, s5, 0
	v_mov_b32_e32 v2, 0x1000
	v_mov_b32_e32 v3, 1
	global_atomic_add v3, v2, v3, s[8:9] offset:1024 sc0
	v_cvt_f32_u32_e32 v2, v17
	v_sub_u32_e32 v4, 0, v17
	v_rcp_iflag_f32_e32 v2, v2
	s_nop 0
	v_mul_f32_e32 v2, 0x4f7ffffe, v2
	v_cvt_u32_f32_e32 v2, v2
	v_mul_lo_u32 v4, v4, v2
	v_mul_hi_u32 v4, v2, v4
	v_add_u32_e32 v2, v2, v4
	s_waitcnt vmcnt(0)
	v_mul_hi_u32 v2, v3, v2
	v_mul_lo_u32 v4, v2, v17
	v_sub_u32_e32 v4, v3, v4
	v_add_u32_e32 v5, 1, v2
	v_cmp_ge_u32_e32 vcc, v4, v17
	v_add_u32_e32 v3, 1, v3
	s_nop 0
	v_cndmask_b32_e32 v2, v2, v5, vcc
	v_sub_u32_e32 v5, v4, v17
	v_cndmask_b32_e32 v4, v4, v5, vcc
	v_add_u32_e32 v5, 1, v2
	v_cmp_ge_u32_e32 vcc, v4, v17
	s_nop 1
	v_cndmask_b32_e32 v2, v2, v5, vcc
	v_mul_lo_u32 v4, v17, v2
	v_add_u32_e32 v4, v4, v17
	v_cmp_ne_u32_e32 vcc, v3, v4
	s_and_saveexec_b64 s[10:11], vcc
	s_xor_b64 s[10:11], exec, s[10:11]
	s_cbranch_execz .LBB0_134
	s_waitcnt lgkmcnt(0)
	v_mov_b32_e32 v1, 0x2000
	buffer_inv sc1
	global_load_dword v1, v1, s[8:9] offset:1024 sc1
	s_add_u32 s16, s8, 0x2400
	s_addc_u32 s17, s9, 0
	s_waitcnt vmcnt(0)
	v_cmp_eq_u32_e32 vcc, v1, v2
	s_and_saveexec_b64 s[12:13], vcc
	s_cbranch_execz .LBB0_133
	v_readlane_b32 s20, v253, 2
	v_readlane_b32 s26, v253, 8
	v_readlane_b32 s27, v253, 9
	s_add_u32 s14, s26, 0x4200
	s_addc_u32 s15, s27, 0
	s_mov_b32 s7, 1
	s_mov_b64 s[18:19], 0
	v_mov_b32_e32 v1, 0
	v_readlane_b32 s21, v253, 3
	v_readlane_b32 s22, v253, 4
	v_readlane_b32 s23, v253, 5
	v_readlane_b32 s24, v253, 6
	v_readlane_b32 s25, v253, 7
	s_branch .LBB0_124

.LBB0_133:
	s_or_b64 exec, exec, s[12:13]
	s_waitcnt vmcnt(0)
	s_waitcnt vmcnt(0)

.LBB0_240:
	s_lshl_b32 s2, s6, 2
	s_add_u32 s2, s4, s2
	s_addc_u32 s3, s5, 0
	v_mov_b32_e32 v2, 0x1000
	v_mov_b32_e32 v3, 1
	global_atomic_add v3, v2, v3, s[2:3] offset:1024 sc0
	v_cvt_f32_u32_e32 v2, v17
	v_sub_u32_e32 v4, 0, v17
	v_rcp_iflag_f32_e32 v2, v2
	s_nop 0
	v_mul_f32_e32 v2, 0x4f7ffffe, v2
	v_cvt_u32_f32_e32 v2, v2
	v_mul_lo_u32 v4, v4, v2
	v_mul_hi_u32 v4, v2, v4
	v_add_u32_e32 v2, v2, v4
	s_waitcnt vmcnt(0)
	v_mul_hi_u32 v2, v3, v2
	v_mul_lo_u32 v4, v2, v17
	v_sub_u32_e32 v4, v3, v4
	v_add_u32_e32 v5, 1, v2
	v_cmp_ge_u32_e32 vcc, v4, v17
	v_add_u32_e32 v3, 1, v3
	s_nop 0
	v_cndmask_b32_e32 v2, v2, v5, vcc
	v_sub_u32_e32 v5, v4, v17
	v_cndmask_b32_e32 v4, v4, v5, vcc
	v_add_u32_e32 v5, 1, v2
	v_cmp_ge_u32_e32 vcc, v4, v17
	s_nop 1
	v_cndmask_b32_e32 v2, v2, v5, vcc
	v_mul_lo_u32 v4, v17, v2
	v_add_u32_e32 v4, v4, v17
	v_cmp_ne_u32_e32 vcc, v3, v4
	s_and_saveexec_b64 s[8:9], vcc
	s_xor_b64 s[8:9], exec, s[8:9]
	s_cbranch_execz .LBB0_254
	s_waitcnt lgkmcnt(0)
	v_mov_b32_e32 v1, 0x2000
	buffer_inv sc1
	global_load_dword v1, v1, s[2:3] offset:1024 sc1
	s_add_u32 s14, s2, 0x2400
	s_addc_u32 s15, s3, 0
	s_waitcnt vmcnt(0)
	v_cmp_eq_u32_e32 vcc, v1, v2
	s_and_saveexec_b64 s[10:11], vcc
	s_cbranch_execz .LBB0_253
	v_readlane_b32 s16, v253, 2
	v_readlane_b32 s22, v253, 8
	v_readlane_b32 s17, v253, 3
	v_readlane_b32 s23, v253, 9
	s_add_u32 s12, s22, 0x4200
	v_readlane_b32 s18, v253, 4
	v_readlane_b32 s19, v253, 5
	s_addc_u32 s13, s23, 0
	s_mov_b32 s7, 1
	s_mov_b64 s[16:17], 0
	v_mov_b32_e32 v1, 0
	v_readlane_b32 s20, v253, 6
	v_readlane_b32 s21, v253, 7
	s_branch .LBB0_244

.LBB0_253:
	s_or_b64 exec, exec, s[10:11]
	s_waitcnt vmcnt(0)
	s_waitcnt vmcnt(0)

.LBB0_321:
	v_readlane_b32 s2, v254, 38
	v_readlane_b32 s3, v254, 39
	v_cvt_f32_u32_e32 v1, v16
	v_sub_u32_e32 v3, 0, v16
	v_rcp_iflag_f32_e32 v1, v1
	s_nop 1
	global_atomic_add v2, v105, v182, s[2:3] sc0
	v_mul_f32_e32 v1, 0x4f7ffffe, v1
	v_cvt_u32_f32_e32 v1, v1
	v_mul_lo_u32 v3, v3, v1
	v_mul_hi_u32 v3, v1, v3
	v_add_u32_e32 v1, v1, v3
	s_waitcnt vmcnt(0)
	v_mul_hi_u32 v1, v2, v1
	v_mul_lo_u32 v3, v1, v16
	v_sub_u32_e32 v3, v2, v3
	v_add_u32_e32 v4, 1, v1
	v_cmp_ge_u32_e32 vcc, v3, v16
	v_add_u32_e32 v2, 1, v2
	s_nop 0
	v_cndmask_b32_e32 v1, v1, v4, vcc
	v_sub_u32_e32 v4, v3, v16
	v_cndmask_b32_e32 v3, v3, v4, vcc
	v_add_u32_e32 v4, 1, v1
	v_cmp_ge_u32_e32 vcc, v3, v16
	s_nop 1
	v_cndmask_b32_e32 v1, v1, v4, vcc
	v_mul_lo_u32 v3, v16, v1
	v_add_u32_e32 v3, v3, v16
	v_cmp_ne_u32_e32 vcc, v2, v3
	s_and_saveexec_b64 s[2:3], vcc
	s_xor_b64 s[2:3], exec, s[2:3]
	s_cbranch_execz .LBB0_335
	v_readlane_b32 s4, v254, 42
	v_readlane_b32 s5, v254, 43
	s_waitcnt lgkmcnt(0)
	s_nop 3
	buffer_inv sc1
	global_load_dword v0, v105, s[4:5] sc1
	s_waitcnt vmcnt(0)
	v_cmp_eq_u32_e32 vcc, v0, v1
	s_and_saveexec_b64 s[4:5], vcc
	s_cbranch_execz .LBB0_334
	s_mov_b32 s17, 1
	s_mov_b64 s[6:7], 0
	s_branch .LBB0_325

.LBB0_334:
	s_or_b64 exec, exec, s[4:5]
	s_waitcnt vmcnt(0)
	s_waitcnt vmcnt(0)

.LBB0_837:
	v_readlane_b32 s2, v254, 38
	v_readlane_b32 s3, v254, 39
	v_cvt_f32_u32_e32 v1, v16
	v_sub_u32_e32 v3, 0, v16
	v_rcp_iflag_f32_e32 v1, v1
	s_nop 1
	global_atomic_add v2, v105, v182, s[2:3] sc0
	v_mul_f32_e32 v1, 0x4f7ffffe, v1
	v_cvt_u32_f32_e32 v1, v1
	v_mul_lo_u32 v3, v3, v1
	v_mul_hi_u32 v3, v1, v3
	v_add_u32_e32 v1, v1, v3
	s_waitcnt vmcnt(0)
	v_mul_hi_u32 v1, v2, v1
	v_mul_lo_u32 v3, v1, v16
	v_sub_u32_e32 v3, v2, v3
	v_add_u32_e32 v4, 1, v1
	v_cmp_ge_u32_e32 vcc, v3, v16
	v_add_u32_e32 v2, 1, v2
	s_nop 0
	v_cndmask_b32_e32 v1, v1, v4, vcc
	v_sub_u32_e32 v4, v3, v16
	v_cndmask_b32_e32 v3, v3, v4, vcc
	v_add_u32_e32 v4, 1, v1
	v_cmp_ge_u32_e32 vcc, v3, v16
	s_nop 1
	v_cndmask_b32_e32 v1, v1, v4, vcc
	v_mul_lo_u32 v3, v16, v1
	v_add_u32_e32 v3, v3, v16
	v_cmp_ne_u32_e32 vcc, v2, v3
	s_and_saveexec_b64 s[2:3], vcc
	s_xor_b64 s[2:3], exec, s[2:3]
	s_cbranch_execz .LBB0_851
	v_readlane_b32 s6, v254, 42
	v_readlane_b32 s7, v254, 43
	s_waitcnt lgkmcnt(0)
	s_nop 3
	buffer_inv sc1
	global_load_dword v0, v105, s[6:7] sc1
	s_waitcnt vmcnt(0)
	v_cmp_eq_u32_e32 vcc, v0, v1
	s_and_saveexec_b64 s[6:7], vcc
	s_cbranch_execz .LBB0_850
	s_mov_b32 s19, 1
	s_mov_b64 s[8:9], 0
	s_branch .LBB0_841

.LBB0_850:
	s_or_b64 exec, exec, s[6:7]
	s_waitcnt vmcnt(0)
	s_waitcnt vmcnt(0)

.LBB0_1207:
	v_readlane_b32 s2, v254, 38
	v_readlane_b32 s3, v254, 39
	v_cvt_f32_u32_e32 v1, v16
	v_sub_u32_e32 v3, 0, v16
	v_rcp_iflag_f32_e32 v1, v1
	s_nop 1
	global_atomic_add v2, v105, v182, s[2:3] sc0
	v_mul_f32_e32 v1, 0x4f7ffffe, v1
	v_cvt_u32_f32_e32 v1, v1
	v_mul_lo_u32 v3, v3, v1
	v_mul_hi_u32 v3, v1, v3
	v_add_u32_e32 v1, v1, v3
	s_waitcnt vmcnt(0)
	v_mul_hi_u32 v1, v2, v1
	v_mul_lo_u32 v3, v1, v16
	v_sub_u32_e32 v3, v2, v3
	v_add_u32_e32 v4, 1, v1
	v_cmp_ge_u32_e32 vcc, v3, v16
	v_add_u32_e32 v2, 1, v2
	s_nop 0
	v_cndmask_b32_e32 v1, v1, v4, vcc
	v_sub_u32_e32 v4, v3, v16
	v_cndmask_b32_e32 v3, v3, v4, vcc
	v_add_u32_e32 v4, 1, v1
	v_cmp_ge_u32_e32 vcc, v3, v16
	s_nop 1
	v_cndmask_b32_e32 v1, v1, v4, vcc
	v_mul_lo_u32 v3, v16, v1
	v_add_u32_e32 v3, v3, v16
	v_cmp_ne_u32_e32 vcc, v2, v3
	s_and_saveexec_b64 s[2:3], vcc
	s_xor_b64 s[2:3], exec, s[2:3]
	s_cbranch_execz .LBB0_1221
	v_readlane_b32 s4, v254, 42
	v_readlane_b32 s5, v254, 43
	s_waitcnt lgkmcnt(0)
	s_nop 3
	buffer_inv sc1
	global_load_dword v0, v105, s[4:5] sc1
	s_waitcnt vmcnt(0)
	v_cmp_eq_u32_e32 vcc, v0, v1
	s_and_saveexec_b64 s[4:5], vcc
	s_cbranch_execz .LBB0_1220
	s_mov_b32 s16, 1
	s_mov_b64 s[6:7], 0
	s_branch .LBB0_1211
